# speedup vs baseline: 1.0109x; 1.0109x over previous
_Z6k_agg1PKiS0_PK6__halfPKfS5_S5_S3_S5_S5_PS1_PfS7_S5_S0_S0_:
	s_and_b32 s3, s2, 7
	s_mul_i32 s5, s3, 0x30d
	s_min_u32 s3, s3, 2
	s_lshr_b32 s2, s2, 3
	v_readfirstlane_b32 s36, v0
	s_add_i32 s2, s3, s2
	s_lshr_b32 s4, s36, 6
	s_add_i32 s2, s2, s5
	s_load_dwordx4 s[8:11], s[0:1], 0x60
	s_lshl_b32 s33, s2, 4
	s_lshl_b32 s2, s4, 2
	v_bfe_u32 v42, v0, 4, 2
	s_add_i32 s2, s2, s33
	v_or_b32_e32 v2, s2, v42
	v_ashrrev_i32_e32 v3, 31, v2
	v_lshlrev_b64 v[10:11], 2, v[2:3]
	s_load_dwordx2 s[2:3], s[0:1], 0x70
	s_waitcnt lgkmcnt(0)
	v_lshl_add_u64 v[2:3], s[10:11], 0, v[10:11]
	global_load_dword v1, v[2:3], off
	s_load_dwordx2 s[6:7], s[0:1], 0x20
	s_load_dwordx2 s[26:27], s[0:1], 0x8
	v_and_b32_e32 v44, 15, v0
	v_lshlrev_b32_e32 v12, 5, v44
	v_lshl_add_u64 v[10:11], s[2:3], 0, v[10:11]
	global_load_dwordx4 v[2:5], v12, s[8:9] offset:16
	global_load_dwordx4 v[6:9], v12, s[8:9]
	global_load_dword v48, v[10:11], off
	v_mov_b32_e32 v33, 0
	v_and_b32_e32 v32, 12, v0
	v_mov_b32_e32 v52, 0x7fffff
	s_waitcnt vmcnt(3)
	v_ashrrev_i32_e32 v46, 24, v1
	v_add_u32_e32 v10, s33, v46
	v_ashrrev_i32_e32 v11, 31, v10
	s_waitcnt lgkmcnt(0)
	v_lshl_add_u64 v[10:11], v[10:11], 4, s[6:7]
	v_lshl_add_u64 v[10:11], v[10:11], 0, v[32:33]
	global_load_dword v50, v[10:11], off
	v_and_b32_e32 v51, 0xffffff, v1
	v_add_u32_e32 v1, v51, v44
	s_waitcnt vmcnt(1)
	v_cmp_lt_i32_e32 vcc, v1, v48
	s_and_saveexec_b64 s[2:3], vcc
	s_cbranch_execz .LBB3_2
	v_lshlrev_b32_e32 v1, 2, v1
	global_load_dword v52, v1, s[26:27]
.LBB3_2:
	s_or_b64 exec, exec, s[2:3]
	s_load_dwordx2 s[20:21], s[0:1], 0x58
	s_load_dwordx2 s[24:25], s[0:1], 0x28
	s_load_dwordx2 s[22:23], s[0:1], 0x40
	v_lshlrev_b32_e32 v49, 3, v44
	v_and_b32_e32 v43, 63, v0
	v_lshlrev_b32_e32 v47, 4, v44
	v_and_b32_e32 v45, 48, v0
	v_cmp_gt_i32_e32 vcc, v48, v51
	v_mov_b32_e32 v32, 0
	v_mov_b32_e32 v35, 0
	v_mov_b32_e32 v34, 0
	v_mov_b32_e32 v37, 0
	v_mov_b32_e32 v36, 0
	v_mov_b32_e32 v39, 0
	v_mov_b32_e32 v38, 0
	v_mov_b32_e32 v64, 0
	s_and_saveexec_b64 s[28:29], vcc
	s_cbranch_execz .LBB3_12
	s_load_dwordx2 s[16:17], s[0:1], 0x10
	s_lshl_b32 s2, s4, 8
	s_addk_i32 s2, 0x1100
	v_cvt_pk_f16_f32 v53, v6, v7
	v_cvt_pk_f16_f32 v54, v8, v9
	v_cvt_pk_f16_f32 v55, v2, v3
	v_cvt_pk_f16_f32 v56, v4, v5
	s_mov_b32 s19, 0x20000
	s_mov_b32 s18, 0x186a000
	s_waitcnt lgkmcnt(0)
	s_and_b32 s17, s17, 0xffff
	v_lshl_or_b32 v57, v43, 2, s2
	v_lshl_or_b32 v58, v45, 2, s2
	v_sub_u32_e32 v59, v48, v51
	v_add_u32_e32 v60, -9, v48
	v_add_u32_e32 v61, -1, v48
	v_mov_b32_e32 v41, 0
	v_mov_b32_e32 v62, 0xff800000
	s_mov_b64 s[30:31], 0
	v_bfrev_b32_e32 v63, 1
	v_mov_b32_e32 v65, 0xff800000
	v_mov_b32_e32 v64, 0
	v_mov_b32_e32 v38, 0
	v_mov_b32_e32 v39, 0
	v_mov_b32_e32 v36, 0
	v_mov_b32_e32 v37, 0
	v_mov_b32_e32 v34, 0
	v_mov_b32_e32 v35, 0
	v_mov_b32_e32 v32, 0
	v_mov_b32_e32 v33, 0
	s_mov_b32 s37, 0x3fb8aa3b
	s_branch .LBB3_5

.LBB3_5:
	v_add_u32_e32 v40, v44, v51
	v_add_u32_e32 v0, 16, v40
	s_waitcnt vmcnt(0)
	v_mul_f32_e32 v77, 0x3fb8aa3b, v50
	ds_write_b32 v57, v52
	v_cmp_lt_i32_e64 s[2:3], v0, v48
	v_mov_b32_e32 v52, 0x7fffff
	s_and_saveexec_b64 s[4:5], s[2:3]
	s_cbranch_execnz .LBB3_8
	s_or_b64 exec, exec, s[4:5]
	v_cmp_lt_i32_e64 s[2:3], 0, v59
	s_and_saveexec_b64 s[34:35], s[2:3]
	s_cbranch_execnz .LBB3_9

.LBB3_9:
	ds_read_b128 v[0:3], v58
	ds_read_b128 v[28:31], v58 offset:16
	v_cmp_lt_u32_e64 s[2:3], 1, v59
	v_cmp_lt_u32_e64 s[4:5], 2, v59
	v_cmp_lt_u32_e64 s[6:7], 3, v59
	v_cmp_lt_u32_e64 s[8:9], 4, v59
	v_cmp_lt_u32_e64 s[10:11], 5, v59
	v_cmp_lt_u32_e64 s[12:13], 6, v59
	v_cmp_lt_u32_e64 s[14:15], 7, v59
	s_waitcnt lgkmcnt(1)
	v_lshl_or_b32 v0, v0, 8, v47
	v_lshl_or_b32 v1, v1, 8, v47
	v_lshl_or_b32 v2, v2, 8, v47
	v_lshl_or_b32 v3, v3, 8, v47
	buffer_load_dwordx4 v[24:27], v0, s[16:19], 0 offen
	buffer_load_dwordx4 v[20:23], v1, s[16:19], 0 offen
	buffer_load_dwordx4 v[16:19], v2, s[16:19], 0 offen
	buffer_load_dwordx4 v[8:11], v3, s[16:19], 0 offen
	s_waitcnt lgkmcnt(0)
	v_lshl_or_b32 v12, v28, 8, v47
	v_lshl_or_b32 v13, v29, 8, v47
	v_lshl_or_b32 v14, v30, 8, v47
	buffer_load_dwordx4 v[4:7], v12, s[16:19], 0 offen
	buffer_load_dwordx4 v[0:3], v13, s[16:19], 0 offen
	v_lshl_or_b32 v28, v31, 8, v47
	buffer_load_dwordx4 v[12:15], v14, s[16:19], 0 offen
	buffer_load_dwordx4 v[28:31], v28, s[16:19], 0 offen
	s_waitcnt vmcnt(7)
	v_dot2_f32_f16 v66, v24, v53, 0
	v_dot2_f32_f16 v66, v25, v54, v66
	v_dot2_f32_f16 v66, v26, v55, v66
	v_dot2_f32_f16 v66, v27, v56, v66
	s_waitcnt vmcnt(6)
	v_dot2_f32_f16 v67, v20, v53, 0
	v_dot2_f32_f16 v67, v21, v54, v67
	v_dot2_f32_f16 v67, v22, v55, v67
	v_dot2_f32_f16 v67, v23, v56, v67
	s_waitcnt vmcnt(5)
	v_dot2_f32_f16 v68, v16, v53, 0
	v_dot2_f32_f16 v68, v17, v54, v68
	v_dot2_f32_f16 v68, v18, v55, v68
	v_dot2_f32_f16 v68, v19, v56, v68
	s_waitcnt vmcnt(4)
	v_dot2_f32_f16 v69, v8, v53, 0
	v_dot2_f32_f16 v69, v9, v54, v69
	v_dot2_f32_f16 v69, v10, v55, v69
	v_dot2_f32_f16 v69, v11, v56, v69
	s_waitcnt vmcnt(3)
	v_dot2_f32_f16 v70, v4, v53, 0
	v_dot2_f32_f16 v70, v5, v54, v70
	v_dot2_f32_f16 v70, v6, v55, v70
	v_dot2_f32_f16 v70, v7, v56, v70
	s_waitcnt vmcnt(2)
	v_dot2_f32_f16 v71, v0, v53, 0
	v_dot2_f32_f16 v71, v1, v54, v71
	v_dot2_f32_f16 v71, v2, v55, v71
	v_dot2_f32_f16 v71, v3, v56, v71
	s_waitcnt vmcnt(1)
	v_dot2_f32_f16 v72, v12, v53, 0
	v_dot2_f32_f16 v72, v13, v54, v72
	v_dot2_f32_f16 v72, v14, v55, v72
	v_dot2_f32_f16 v72, v15, v56, v72
	s_waitcnt vmcnt(0)
	v_dot2_f32_f16 v73, v28, v53, 0
	v_dot2_f32_f16 v73, v29, v54, v73
	v_dot2_f32_f16 v73, v30, v55, v73
	v_dot2_f32_f16 v73, v31, v56, v73
	s_nop 1
	v_add_f32_dpp v66, v66, v66 quad_perm:[1,0,3,2] row_mask:0xf bank_mask:0xf bound_ctrl:1
	v_add_f32_dpp v67, v67, v67 quad_perm:[1,0,3,2] row_mask:0xf bank_mask:0xf bound_ctrl:1
	v_add_f32_dpp v68, v68, v68 quad_perm:[1,0,3,2] row_mask:0xf bank_mask:0xf bound_ctrl:1
	v_add_f32_dpp v69, v69, v69 quad_perm:[1,0,3,2] row_mask:0xf bank_mask:0xf bound_ctrl:1
	v_add_f32_dpp v70, v70, v70 quad_perm:[1,0,3,2] row_mask:0xf bank_mask:0xf bound_ctrl:1
	v_add_f32_dpp v71, v71, v71 quad_perm:[1,0,3,2] row_mask:0xf bank_mask:0xf bound_ctrl:1
	v_add_f32_dpp v72, v72, v72 quad_perm:[1,0,3,2] row_mask:0xf bank_mask:0xf bound_ctrl:1
	v_add_f32_dpp v73, v73, v73 quad_perm:[1,0,3,2] row_mask:0xf bank_mask:0xf bound_ctrl:1
	v_add_f32_dpp v66, v66, v66 quad_perm:[2,3,0,1] row_mask:0xf bank_mask:0xf bound_ctrl:1
	v_add_f32_dpp v67, v67, v67 quad_perm:[2,3,0,1] row_mask:0xf bank_mask:0xf bound_ctrl:1
	v_add_f32_dpp v68, v68, v68 quad_perm:[2,3,0,1] row_mask:0xf bank_mask:0xf bound_ctrl:1
	v_add_f32_dpp v69, v69, v69 quad_perm:[2,3,0,1] row_mask:0xf bank_mask:0xf bound_ctrl:1
	v_add_f32_dpp v70, v70, v70 quad_perm:[2,3,0,1] row_mask:0xf bank_mask:0xf bound_ctrl:1
	v_add_f32_dpp v71, v71, v71 quad_perm:[2,3,0,1] row_mask:0xf bank_mask:0xf bound_ctrl:1
	v_add_f32_dpp v72, v72, v72 quad_perm:[2,3,0,1] row_mask:0xf bank_mask:0xf bound_ctrl:1
	v_add_f32_dpp v73, v73, v73 quad_perm:[2,3,0,1] row_mask:0xf bank_mask:0xf bound_ctrl:1
	v_fma_f32 v66, v66, s37, v77
	v_fma_f32 v67, v67, s37, v77
	v_fma_f32 v68, v68, s37, v77
	v_fma_f32 v69, v69, s37, v77
	v_fma_f32 v70, v70, s37, v77
	v_fma_f32 v71, v71, s37, v77
	v_fma_f32 v72, v72, s37, v77
	v_fma_f32 v73, v73, s37, v77
	v_mul_f32_e32 v74, 0x3e4ccccd, v66
	v_mul_f32_e32 v75, 0x3e4ccccd, v67
	v_max_f32_e32 v66, v66, v74
	v_mul_f32_e32 v74, 0x3e4ccccd, v68
	v_max_f32_e32 v67, v67, v75
	v_mul_f32_e32 v75, 0x3e4ccccd, v69
	v_max_f32_e32 v68, v68, v74
	v_mul_f32_e32 v74, 0x3e4ccccd, v70
	v_max_f32_e32 v69, v69, v75
	v_mul_f32_e32 v75, 0x3e4ccccd, v71
	v_max_f32_e32 v70, v70, v74
	v_mul_f32_e32 v74, 0x3e4ccccd, v72
	v_max_f32_e32 v71, v71, v75
	v_mul_f32_e32 v75, 0x3e4ccccd, v73
	v_max_f32_e32 v72, v72, v74
	v_max_f32_e32 v73, v73, v75
	v_cndmask_b32_e64 v67, v62, v67, s[2:3]
	v_cndmask_b32_e64 v68, v62, v68, s[4:5]
	v_cndmask_b32_e64 v69, v62, v69, s[6:7]
	v_cndmask_b32_e64 v70, v62, v70, s[8:9]
	v_cndmask_b32_e64 v71, v62, v71, s[10:11]
	v_cndmask_b32_e64 v72, v62, v72, s[12:13]
	v_cndmask_b32_e64 v73, v62, v73, s[14:15]
	v_max3_f32 v40, v66, v67, v68
	v_max3_f32 v40, v40, v69, v70
	v_max3_f32 v40, v40, v71, v72
	v_max3_f32 v40, v40, v73, v65
	v_sub_f32_e32 v76, v65, v40
	v_exp_f32_e32 v76, v76
	v_sub_f32_e32 v66, v66, v40
	v_sub_f32_e32 v67, v67, v40
	v_sub_f32_e32 v68, v68, v40
	v_sub_f32_e32 v69, v69, v40
	v_sub_f32_e32 v70, v70, v40
	v_sub_f32_e32 v71, v71, v40
	v_sub_f32_e32 v72, v72, v40
	v_sub_f32_e32 v73, v73, v40
	v_exp_f32_e32 v66, v66
	v_exp_f32_e32 v67, v67
	v_exp_f32_e32 v68, v68
	v_exp_f32_e32 v69, v69
	v_exp_f32_e32 v70, v70
	v_exp_f32_e32 v71, v71
	v_exp_f32_e32 v72, v72
	v_exp_f32_e32 v73, v73
	v_mul_f32_e32 v38, v76, v38
	v_mul_f32_e32 v39, v76, v39
	v_mul_f32_e32 v36, v76, v36
	v_mul_f32_e32 v37, v76, v37
	v_mul_f32_e32 v34, v76, v34
	v_mul_f32_e32 v35, v76, v35
	v_mul_f32_e32 v32, v76, v32
	v_mul_f32_e32 v33, v76, v33
	v_mul_f32_e32 v64, v76, v64
	v_mov_b32_e32 v65, v40
	v_fma_mix_f32 v38, v24, v66, v38 op_sel:[0,0,0] op_sel_hi:[1,0,0]
	v_fma_mix_f32 v39, v24, v66, v39 op_sel:[1,0,0] op_sel_hi:[1,0,0]
	v_fma_mix_f32 v36, v25, v66, v36 op_sel:[0,0,0] op_sel_hi:[1,0,0]
	v_fma_mix_f32 v37, v25, v66, v37 op_sel:[1,0,0] op_sel_hi:[1,0,0]
	v_fma_mix_f32 v34, v26, v66, v34 op_sel:[0,0,0] op_sel_hi:[1,0,0]
	v_fma_mix_f32 v35, v26, v66, v35 op_sel:[1,0,0] op_sel_hi:[1,0,0]
	v_fma_mix_f32 v32, v27, v66, v32 op_sel:[0,0,0] op_sel_hi:[1,0,0]
	v_fma_mix_f32 v33, v27, v66, v33 op_sel:[1,0,0] op_sel_hi:[1,0,0]
	v_add_f32_e32 v64, v64, v66
	v_fma_mix_f32 v38, v20, v67, v38 op_sel:[0,0,0] op_sel_hi:[1,0,0]
	v_fma_mix_f32 v39, v20, v67, v39 op_sel:[1,0,0] op_sel_hi:[1,0,0]
	v_fma_mix_f32 v36, v21, v67, v36 op_sel:[0,0,0] op_sel_hi:[1,0,0]
	v_fma_mix_f32 v37, v21, v67, v37 op_sel:[1,0,0] op_sel_hi:[1,0,0]
	v_fma_mix_f32 v34, v22, v67, v34 op_sel:[0,0,0] op_sel_hi:[1,0,0]
	v_fma_mix_f32 v35, v22, v67, v35 op_sel:[1,0,0] op_sel_hi:[1,0,0]
	v_fma_mix_f32 v32, v23, v67, v32 op_sel:[0,0,0] op_sel_hi:[1,0,0]
	v_fma_mix_f32 v33, v23, v67, v33 op_sel:[1,0,0] op_sel_hi:[1,0,0]
	v_add_f32_e32 v64, v64, v67
	v_fma_mix_f32 v38, v16, v68, v38 op_sel:[0,0,0] op_sel_hi:[1,0,0]
	v_fma_mix_f32 v39, v16, v68, v39 op_sel:[1,0,0] op_sel_hi:[1,0,0]
	v_fma_mix_f32 v36, v17, v68, v36 op_sel:[0,0,0] op_sel_hi:[1,0,0]
	v_fma_mix_f32 v37, v17, v68, v37 op_sel:[1,0,0] op_sel_hi:[1,0,0]
	v_fma_mix_f32 v34, v18, v68, v34 op_sel:[0,0,0] op_sel_hi:[1,0,0]
	v_fma_mix_f32 v35, v18, v68, v35 op_sel:[1,0,0] op_sel_hi:[1,0,0]
	v_fma_mix_f32 v32, v19, v68, v32 op_sel:[0,0,0] op_sel_hi:[1,0,0]
	v_fma_mix_f32 v33, v19, v68, v33 op_sel:[1,0,0] op_sel_hi:[1,0,0]
	v_add_f32_e32 v64, v64, v68
	v_fma_mix_f32 v38, v8, v69, v38 op_sel:[0,0,0] op_sel_hi:[1,0,0]
	v_fma_mix_f32 v39, v8, v69, v39 op_sel:[1,0,0] op_sel_hi:[1,0,0]
	v_fma_mix_f32 v36, v9, v69, v36 op_sel:[0,0,0] op_sel_hi:[1,0,0]
	v_fma_mix_f32 v37, v9, v69, v37 op_sel:[1,0,0] op_sel_hi:[1,0,0]
	v_fma_mix_f32 v34, v10, v69, v34 op_sel:[0,0,0] op_sel_hi:[1,0,0]
	v_fma_mix_f32 v35, v10, v69, v35 op_sel:[1,0,0] op_sel_hi:[1,0,0]
	v_fma_mix_f32 v32, v11, v69, v32 op_sel:[0,0,0] op_sel_hi:[1,0,0]
	v_fma_mix_f32 v33, v11, v69, v33 op_sel:[1,0,0] op_sel_hi:[1,0,0]
	v_add_f32_e32 v64, v64, v69
	v_fma_mix_f32 v38, v4, v70, v38 op_sel:[0,0,0] op_sel_hi:[1,0,0]
	v_fma_mix_f32 v39, v4, v70, v39 op_sel:[1,0,0] op_sel_hi:[1,0,0]
	v_fma_mix_f32 v36, v5, v70, v36 op_sel:[0,0,0] op_sel_hi:[1,0,0]
	v_fma_mix_f32 v37, v5, v70, v37 op_sel:[1,0,0] op_sel_hi:[1,0,0]
	v_fma_mix_f32 v34, v6, v70, v34 op_sel:[0,0,0] op_sel_hi:[1,0,0]
	v_fma_mix_f32 v35, v6, v70, v35 op_sel:[1,0,0] op_sel_hi:[1,0,0]
	v_fma_mix_f32 v32, v7, v70, v32 op_sel:[0,0,0] op_sel_hi:[1,0,0]
	v_fma_mix_f32 v33, v7, v70, v33 op_sel:[1,0,0] op_sel_hi:[1,0,0]
	v_add_f32_e32 v64, v64, v70
	v_fma_mix_f32 v38, v0, v71, v38 op_sel:[0,0,0] op_sel_hi:[1,0,0]
	v_fma_mix_f32 v39, v0, v71, v39 op_sel:[1,0,0] op_sel_hi:[1,0,0]
	v_fma_mix_f32 v36, v1, v71, v36 op_sel:[0,0,0] op_sel_hi:[1,0,0]
	v_fma_mix_f32 v37, v1, v71, v37 op_sel:[1,0,0] op_sel_hi:[1,0,0]
	v_fma_mix_f32 v34, v2, v71, v34 op_sel:[0,0,0] op_sel_hi:[1,0,0]
	v_fma_mix_f32 v35, v2, v71, v35 op_sel:[1,0,0] op_sel_hi:[1,0,0]
	v_fma_mix_f32 v32, v3, v71, v32 op_sel:[0,0,0] op_sel_hi:[1,0,0]
	v_fma_mix_f32 v33, v3, v71, v33 op_sel:[1,0,0] op_sel_hi:[1,0,0]
	v_add_f32_e32 v64, v64, v71
	v_fma_mix_f32 v38, v12, v72, v38 op_sel:[0,0,0] op_sel_hi:[1,0,0]
	v_fma_mix_f32 v39, v12, v72, v39 op_sel:[1,0,0] op_sel_hi:[1,0,0]
	v_fma_mix_f32 v36, v13, v72, v36 op_sel:[0,0,0] op_sel_hi:[1,0,0]
	v_fma_mix_f32 v37, v13, v72, v37 op_sel:[1,0,0] op_sel_hi:[1,0,0]
	v_fma_mix_f32 v34, v14, v72, v34 op_sel:[0,0,0] op_sel_hi:[1,0,0]
	v_fma_mix_f32 v35, v14, v72, v35 op_sel:[1,0,0] op_sel_hi:[1,0,0]
	v_fma_mix_f32 v32, v15, v72, v32 op_sel:[0,0,0] op_sel_hi:[1,0,0]
	v_fma_mix_f32 v33, v15, v72, v33 op_sel:[1,0,0] op_sel_hi:[1,0,0]
	v_add_f32_e32 v64, v64, v72
	v_fma_mix_f32 v38, v28, v73, v38 op_sel:[0,0,0] op_sel_hi:[1,0,0]
	v_fma_mix_f32 v39, v28, v73, v39 op_sel:[1,0,0] op_sel_hi:[1,0,0]
	v_fma_mix_f32 v36, v29, v73, v36 op_sel:[0,0,0] op_sel_hi:[1,0,0]
	v_fma_mix_f32 v37, v29, v73, v37 op_sel:[1,0,0] op_sel_hi:[1,0,0]
	v_fma_mix_f32 v34, v30, v73, v34 op_sel:[0,0,0] op_sel_hi:[1,0,0]
	v_fma_mix_f32 v35, v30, v73, v35 op_sel:[1,0,0] op_sel_hi:[1,0,0]
	v_fma_mix_f32 v32, v31, v73, v32 op_sel:[0,0,0] op_sel_hi:[1,0,0]
	v_fma_mix_f32 v33, v31, v73, v33 op_sel:[1,0,0] op_sel_hi:[1,0,0]
	v_add_f32_e32 v64, v64, v73
	s_or_b64 exec, exec, s[34:35]
	v_cmp_lt_i32_e64 s[2:3], 8, v59
	s_and_saveexec_b64 s[34:35], s[2:3]
	s_cbranch_execz .LBB3_4
.LBB3_10:
	ds_read_b128 v[0:3], v58 offset:32
	ds_read_b128 v[28:31], v58 offset:48
	v_cmp_lt_u32_e64 s[2:3], 9, v59
	v_cmp_lt_u32_e64 s[4:5], 10, v59
	v_cmp_lt_u32_e64 s[6:7], 11, v59
	v_cmp_lt_u32_e64 s[8:9], 12, v59
	v_cmp_lt_u32_e64 s[10:11], 13, v59
	v_cmp_lt_u32_e64 s[12:13], 14, v59
	v_cmp_lt_u32_e64 s[14:15], 15, v59
	s_waitcnt lgkmcnt(1)
	v_lshl_or_b32 v0, v0, 8, v47
	v_lshl_or_b32 v1, v1, 8, v47
	v_lshl_or_b32 v2, v2, 8, v47
	v_lshl_or_b32 v3, v3, 8, v47
	buffer_load_dwordx4 v[24:27], v0, s[16:19], 0 offen
	buffer_load_dwordx4 v[20:23], v1, s[16:19], 0 offen
	buffer_load_dwordx4 v[16:19], v2, s[16:19], 0 offen
	buffer_load_dwordx4 v[8:11], v3, s[16:19], 0 offen
	s_waitcnt lgkmcnt(0)
	v_lshl_or_b32 v12, v28, 8, v47
	v_lshl_or_b32 v13, v29, 8, v47
	v_lshl_or_b32 v14, v30, 8, v47
	buffer_load_dwordx4 v[4:7], v12, s[16:19], 0 offen
	buffer_load_dwordx4 v[0:3], v13, s[16:19], 0 offen
	v_lshl_or_b32 v28, v31, 8, v47
	buffer_load_dwordx4 v[12:15], v14, s[16:19], 0 offen
	buffer_load_dwordx4 v[28:31], v28, s[16:19], 0 offen
	s_waitcnt vmcnt(7)
	v_dot2_f32_f16 v66, v24, v53, 0
	v_dot2_f32_f16 v66, v25, v54, v66
	v_dot2_f32_f16 v66, v26, v55, v66
	v_dot2_f32_f16 v66, v27, v56, v66
	s_waitcnt vmcnt(6)
	v_dot2_f32_f16 v67, v20, v53, 0
	v_dot2_f32_f16 v67, v21, v54, v67
	v_dot2_f32_f16 v67, v22, v55, v67
	v_dot2_f32_f16 v67, v23, v56, v67
	s_waitcnt vmcnt(5)
	v_dot2_f32_f16 v68, v16, v53, 0
	v_dot2_f32_f16 v68, v17, v54, v68
	v_dot2_f32_f16 v68, v18, v55, v68
	v_dot2_f32_f16 v68, v19, v56, v68
	s_waitcnt vmcnt(4)
	v_dot2_f32_f16 v69, v8, v53, 0
	v_dot2_f32_f16 v69, v9, v54, v69
	v_dot2_f32_f16 v69, v10, v55, v69
	v_dot2_f32_f16 v69, v11, v56, v69
	s_waitcnt vmcnt(3)
	v_dot2_f32_f16 v70, v4, v53, 0
	v_dot2_f32_f16 v70, v5, v54, v70
	v_dot2_f32_f16 v70, v6, v55, v70
	v_dot2_f32_f16 v70, v7, v56, v70
	s_waitcnt vmcnt(2)
	v_dot2_f32_f16 v71, v0, v53, 0
	v_dot2_f32_f16 v71, v1, v54, v71
	v_dot2_f32_f16 v71, v2, v55, v71
	v_dot2_f32_f16 v71, v3, v56, v71
	s_waitcnt vmcnt(1)
	v_dot2_f32_f16 v72, v12, v53, 0
	v_dot2_f32_f16 v72, v13, v54, v72
	v_dot2_f32_f16 v72, v14, v55, v72
	v_dot2_f32_f16 v72, v15, v56, v72
	s_waitcnt vmcnt(0)
	v_dot2_f32_f16 v73, v28, v53, 0
	v_dot2_f32_f16 v73, v29, v54, v73
	v_dot2_f32_f16 v73, v30, v55, v73
	v_dot2_f32_f16 v73, v31, v56, v73
	s_nop 1
	v_add_f32_dpp v66, v66, v66 quad_perm:[1,0,3,2] row_mask:0xf bank_mask:0xf bound_ctrl:1
	v_add_f32_dpp v67, v67, v67 quad_perm:[1,0,3,2] row_mask:0xf bank_mask:0xf bound_ctrl:1
	v_add_f32_dpp v68, v68, v68 quad_perm:[1,0,3,2] row_mask:0xf bank_mask:0xf bound_ctrl:1
	v_add_f32_dpp v69, v69, v69 quad_perm:[1,0,3,2] row_mask:0xf bank_mask:0xf bound_ctrl:1
	v_add_f32_dpp v70, v70, v70 quad_perm:[1,0,3,2] row_mask:0xf bank_mask:0xf bound_ctrl:1
	v_add_f32_dpp v71, v71, v71 quad_perm:[1,0,3,2] row_mask:0xf bank_mask:0xf bound_ctrl:1
	v_add_f32_dpp v72, v72, v72 quad_perm:[1,0,3,2] row_mask:0xf bank_mask:0xf bound_ctrl:1
	v_add_f32_dpp v73, v73, v73 quad_perm:[1,0,3,2] row_mask:0xf bank_mask:0xf bound_ctrl:1
	v_add_f32_dpp v66, v66, v66 quad_perm:[2,3,0,1] row_mask:0xf bank_mask:0xf bound_ctrl:1
	v_add_f32_dpp v67, v67, v67 quad_perm:[2,3,0,1] row_mask:0xf bank_mask:0xf bound_ctrl:1
	v_add_f32_dpp v68, v68, v68 quad_perm:[2,3,0,1] row_mask:0xf bank_mask:0xf bound_ctrl:1
	v_add_f32_dpp v69, v69, v69 quad_perm:[2,3,0,1] row_mask:0xf bank_mask:0xf bound_ctrl:1
	v_add_f32_dpp v70, v70, v70 quad_perm:[2,3,0,1] row_mask:0xf bank_mask:0xf bound_ctrl:1
	v_add_f32_dpp v71, v71, v71 quad_perm:[2,3,0,1] row_mask:0xf bank_mask:0xf bound_ctrl:1
	v_add_f32_dpp v72, v72, v72 quad_perm:[2,3,0,1] row_mask:0xf bank_mask:0xf bound_ctrl:1
	v_add_f32_dpp v73, v73, v73 quad_perm:[2,3,0,1] row_mask:0xf bank_mask:0xf bound_ctrl:1
	v_fma_f32 v66, v66, s37, v77
	v_fma_f32 v67, v67, s37, v77
	v_fma_f32 v68, v68, s37, v77
	v_fma_f32 v69, v69, s37, v77
	v_fma_f32 v70, v70, s37, v77
	v_fma_f32 v71, v71, s37, v77
	v_fma_f32 v72, v72, s37, v77
	v_fma_f32 v73, v73, s37, v77
	v_mul_f32_e32 v74, 0x3e4ccccd, v66
	v_mul_f32_e32 v75, 0x3e4ccccd, v67
	v_max_f32_e32 v66, v66, v74
	v_mul_f32_e32 v74, 0x3e4ccccd, v68
	v_max_f32_e32 v67, v67, v75
	v_mul_f32_e32 v75, 0x3e4ccccd, v69
	v_max_f32_e32 v68, v68, v74
	v_mul_f32_e32 v74, 0x3e4ccccd, v70
	v_max_f32_e32 v69, v69, v75
	v_mul_f32_e32 v75, 0x3e4ccccd, v71
	v_max_f32_e32 v70, v70, v74
	v_mul_f32_e32 v74, 0x3e4ccccd, v72
	v_max_f32_e32 v71, v71, v75
	v_mul_f32_e32 v75, 0x3e4ccccd, v73
	v_max_f32_e32 v72, v72, v74
	v_max_f32_e32 v73, v73, v75
	v_cndmask_b32_e64 v67, v62, v67, s[2:3]
	v_cndmask_b32_e64 v68, v62, v68, s[4:5]
	v_cndmask_b32_e64 v69, v62, v69, s[6:7]
	v_cndmask_b32_e64 v70, v62, v70, s[8:9]
	v_cndmask_b32_e64 v71, v62, v71, s[10:11]
	v_cndmask_b32_e64 v72, v62, v72, s[12:13]
	v_cndmask_b32_e64 v73, v62, v73, s[14:15]
	v_max3_f32 v40, v66, v67, v68
	v_max3_f32 v40, v40, v69, v70
	v_max3_f32 v40, v40, v71, v72
	v_max3_f32 v40, v40, v73, v65
	v_sub_f32_e32 v76, v65, v40
	v_exp_f32_e32 v76, v76
	v_sub_f32_e32 v66, v66, v40
	v_sub_f32_e32 v67, v67, v40
	v_sub_f32_e32 v68, v68, v40
	v_sub_f32_e32 v69, v69, v40
	v_sub_f32_e32 v70, v70, v40
	v_sub_f32_e32 v71, v71, v40
	v_sub_f32_e32 v72, v72, v40
	v_sub_f32_e32 v73, v73, v40
	v_exp_f32_e32 v66, v66
	v_exp_f32_e32 v67, v67
	v_exp_f32_e32 v68, v68
	v_exp_f32_e32 v69, v69
	v_exp_f32_e32 v70, v70
	v_exp_f32_e32 v71, v71
	v_exp_f32_e32 v72, v72
	v_exp_f32_e32 v73, v73
	v_mul_f32_e32 v38, v76, v38
	v_mul_f32_e32 v39, v76, v39
	v_mul_f32_e32 v36, v76, v36
	v_mul_f32_e32 v37, v76, v37
	v_mul_f32_e32 v34, v76, v34
	v_mul_f32_e32 v35, v76, v35
	v_mul_f32_e32 v32, v76, v32
	v_mul_f32_e32 v33, v76, v33
	v_mul_f32_e32 v64, v76, v64
	v_mov_b32_e32 v65, v40
	v_fma_mix_f32 v38, v24, v66, v38 op_sel:[0,0,0] op_sel_hi:[1,0,0]
	v_fma_mix_f32 v39, v24, v66, v39 op_sel:[1,0,0] op_sel_hi:[1,0,0]
	v_fma_mix_f32 v36, v25, v66, v36 op_sel:[0,0,0] op_sel_hi:[1,0,0]
	v_fma_mix_f32 v37, v25, v66, v37 op_sel:[1,0,0] op_sel_hi:[1,0,0]
	v_fma_mix_f32 v34, v26, v66, v34 op_sel:[0,0,0] op_sel_hi:[1,0,0]
	v_fma_mix_f32 v35, v26, v66, v35 op_sel:[1,0,0] op_sel_hi:[1,0,0]
	v_fma_mix_f32 v32, v27, v66, v32 op_sel:[0,0,0] op_sel_hi:[1,0,0]
	v_fma_mix_f32 v33, v27, v66, v33 op_sel:[1,0,0] op_sel_hi:[1,0,0]
	v_add_f32_e32 v64, v64, v66
	v_fma_mix_f32 v38, v20, v67, v38 op_sel:[0,0,0] op_sel_hi:[1,0,0]
	v_fma_mix_f32 v39, v20, v67, v39 op_sel:[1,0,0] op_sel_hi:[1,0,0]
	v_fma_mix_f32 v36, v21, v67, v36 op_sel:[0,0,0] op_sel_hi:[1,0,0]
	v_fma_mix_f32 v37, v21, v67, v37 op_sel:[1,0,0] op_sel_hi:[1,0,0]
	v_fma_mix_f32 v34, v22, v67, v34 op_sel:[0,0,0] op_sel_hi:[1,0,0]
	v_fma_mix_f32 v35, v22, v67, v35 op_sel:[1,0,0] op_sel_hi:[1,0,0]
	v_fma_mix_f32 v32, v23, v67, v32 op_sel:[0,0,0] op_sel_hi:[1,0,0]
	v_fma_mix_f32 v33, v23, v67, v33 op_sel:[1,0,0] op_sel_hi:[1,0,0]
	v_add_f32_e32 v64, v64, v67
	v_fma_mix_f32 v38, v16, v68, v38 op_sel:[0,0,0] op_sel_hi:[1,0,0]
	v_fma_mix_f32 v39, v16, v68, v39 op_sel:[1,0,0] op_sel_hi:[1,0,0]
	v_fma_mix_f32 v36, v17, v68, v36 op_sel:[0,0,0] op_sel_hi:[1,0,0]
	v_fma_mix_f32 v37, v17, v68, v37 op_sel:[1,0,0] op_sel_hi:[1,0,0]
	v_fma_mix_f32 v34, v18, v68, v34 op_sel:[0,0,0] op_sel_hi:[1,0,0]
	v_fma_mix_f32 v35, v18, v68, v35 op_sel:[1,0,0] op_sel_hi:[1,0,0]
	v_fma_mix_f32 v32, v19, v68, v32 op_sel:[0,0,0] op_sel_hi:[1,0,0]
	v_fma_mix_f32 v33, v19, v68, v33 op_sel:[1,0,0] op_sel_hi:[1,0,0]
	v_add_f32_e32 v64, v64, v68
	v_fma_mix_f32 v38, v8, v69, v38 op_sel:[0,0,0] op_sel_hi:[1,0,0]
	v_fma_mix_f32 v39, v8, v69, v39 op_sel:[1,0,0] op_sel_hi:[1,0,0]
	v_fma_mix_f32 v36, v9, v69, v36 op_sel:[0,0,0] op_sel_hi:[1,0,0]
	v_fma_mix_f32 v37, v9, v69, v37 op_sel:[1,0,0] op_sel_hi:[1,0,0]
	v_fma_mix_f32 v34, v10, v69, v34 op_sel:[0,0,0] op_sel_hi:[1,0,0]
	v_fma_mix_f32 v35, v10, v69, v35 op_sel:[1,0,0] op_sel_hi:[1,0,0]
	v_fma_mix_f32 v32, v11, v69, v32 op_sel:[0,0,0] op_sel_hi:[1,0,0]
	v_fma_mix_f32 v33, v11, v69, v33 op_sel:[1,0,0] op_sel_hi:[1,0,0]
	v_add_f32_e32 v64, v64, v69
	v_fma_mix_f32 v38, v4, v70, v38 op_sel:[0,0,0] op_sel_hi:[1,0,0]
	v_fma_mix_f32 v39, v4, v70, v39 op_sel:[1,0,0] op_sel_hi:[1,0,0]
	v_fma_mix_f32 v36, v5, v70, v36 op_sel:[0,0,0] op_sel_hi:[1,0,0]
	v_fma_mix_f32 v37, v5, v70, v37 op_sel:[1,0,0] op_sel_hi:[1,0,0]
	v_fma_mix_f32 v34, v6, v70, v34 op_sel:[0,0,0] op_sel_hi:[1,0,0]
	v_fma_mix_f32 v35, v6, v70, v35 op_sel:[1,0,0] op_sel_hi:[1,0,0]
	v_fma_mix_f32 v32, v7, v70, v32 op_sel:[0,0,0] op_sel_hi:[1,0,0]
	v_fma_mix_f32 v33, v7, v70, v33 op_sel:[1,0,0] op_sel_hi:[1,0,0]
	v_add_f32_e32 v64, v64, v70
	v_fma_mix_f32 v38, v0, v71, v38 op_sel:[0,0,0] op_sel_hi:[1,0,0]
	v_fma_mix_f32 v39, v0, v71, v39 op_sel:[1,0,0] op_sel_hi:[1,0,0]
	v_fma_mix_f32 v36, v1, v71, v36 op_sel:[0,0,0] op_sel_hi:[1,0,0]
	v_fma_mix_f32 v37, v1, v71, v37 op_sel:[1,0,0] op_sel_hi:[1,0,0]
	v_fma_mix_f32 v34, v2, v71, v34 op_sel:[0,0,0] op_sel_hi:[1,0,0]
	v_fma_mix_f32 v35, v2, v71, v35 op_sel:[1,0,0] op_sel_hi:[1,0,0]
	v_fma_mix_f32 v32, v3, v71, v32 op_sel:[0,0,0] op_sel_hi:[1,0,0]
	v_fma_mix_f32 v33, v3, v71, v33 op_sel:[1,0,0] op_sel_hi:[1,0,0]
	v_add_f32_e32 v64, v64, v71
	v_fma_mix_f32 v38, v12, v72, v38 op_sel:[0,0,0] op_sel_hi:[1,0,0]
	v_fma_mix_f32 v39, v12, v72, v39 op_sel:[1,0,0] op_sel_hi:[1,0,0]
	v_fma_mix_f32 v36, v13, v72, v36 op_sel:[0,0,0] op_sel_hi:[1,0,0]
	v_fma_mix_f32 v37, v13, v72, v37 op_sel:[1,0,0] op_sel_hi:[1,0,0]
	v_fma_mix_f32 v34, v14, v72, v34 op_sel:[0,0,0] op_sel_hi:[1,0,0]
	v_fma_mix_f32 v35, v14, v72, v35 op_sel:[1,0,0] op_sel_hi:[1,0,0]
	v_fma_mix_f32 v32, v15, v72, v32 op_sel:[0,0,0] op_sel_hi:[1,0,0]
	v_fma_mix_f32 v33, v15, v72, v33 op_sel:[1,0,0] op_sel_hi:[1,0,0]
	v_add_f32_e32 v64, v64, v72
	v_fma_mix_f32 v38, v28, v73, v38 op_sel:[0,0,0] op_sel_hi:[1,0,0]
	v_fma_mix_f32 v39, v28, v73, v39 op_sel:[1,0,0] op_sel_hi:[1,0,0]
	v_fma_mix_f32 v36, v29, v73, v36 op_sel:[0,0,0] op_sel_hi:[1,0,0]
	v_fma_mix_f32 v37, v29, v73, v37 op_sel:[1,0,0] op_sel_hi:[1,0,0]
	v_fma_mix_f32 v34, v30, v73, v34 op_sel:[0,0,0] op_sel_hi:[1,0,0]
	v_fma_mix_f32 v35, v30, v73, v35 op_sel:[1,0,0] op_sel_hi:[1,0,0]
	v_fma_mix_f32 v32, v31, v73, v32 op_sel:[0,0,0] op_sel_hi:[1,0,0]
	v_fma_mix_f32 v33, v31, v73, v33 op_sel:[1,0,0] op_sel_hi:[1,0,0]
	v_add_f32_e32 v64, v64, v73
	s_branch .LBB3_4

	.amdhsa_kernel _Z6k_agg1PKiS0_PK6__halfPKfS5_S5_S3_S5_S5_PS1_PfS7_S5_S0_S0_
		.amdhsa_group_segment_fixed_size 5376
		.amdhsa_private_segment_fixed_size 0
		.amdhsa_kernarg_size 120
		.amdhsa_user_sgpr_count 2
		.amdhsa_user_sgpr_dispatch_ptr 0
		.amdhsa_user_sgpr_queue_ptr 0
		.amdhsa_user_sgpr_kernarg_segment_ptr 1
		.amdhsa_user_sgpr_dispatch_id 0
		.amdhsa_user_sgpr_kernarg_preload_length 0
		.amdhsa_user_sgpr_kernarg_preload_offset 0
		.amdhsa_user_sgpr_private_segment_size 0
		.amdhsa_uses_dynamic_stack 0
		.amdhsa_enable_private_segment 0
		.amdhsa_system_sgpr_workgroup_id_x 1
		.amdhsa_system_sgpr_workgroup_id_y 0
		.amdhsa_system_sgpr_workgroup_id_z 0
		.amdhsa_system_sgpr_workgroup_info 0
		.amdhsa_system_vgpr_workitem_id 0
		.amdhsa_next_free_vgpr 78
		.amdhsa_next_free_sgpr 38
		.amdhsa_accum_offset 80
		.amdhsa_reserve_vcc 1
		.amdhsa_float_round_mode_32 0
		.amdhsa_float_round_mode_16_64 0
		.amdhsa_float_denorm_mode_32 3
		.amdhsa_float_denorm_mode_16_64 3
		.amdhsa_dx10_clamp 1
		.amdhsa_ieee_mode 1
		.amdhsa_fp16_overflow 0
		.amdhsa_tg_split 0
		.amdhsa_exception_fp_ieee_invalid_op 0
		.amdhsa_exception_fp_denorm_src 0
		.amdhsa_exception_fp_ieee_div_zero 0
		.amdhsa_exception_fp_ieee_overflow 0
		.amdhsa_exception_fp_ieee_underflow 0
		.amdhsa_exception_fp_ieee_inexact 0
		.amdhsa_exception_int_div_zero 0
	.end_amdhsa_kernel

amdhsa.kernels:
  - .agpr_count:     0
    .args:
      - .actual_access:  read_only
        .address_space:  global
        .offset:         0
        .size:           8
        .value_kind:     global_buffer
      - .actual_access:  read_only
        .address_space:  global
        .offset:         8
        .size:           8
        .value_kind:     global_buffer
      - .actual_access:  write_only
        .address_space:  global
        .offset:         16
        .size:           8
        .value_kind:     global_buffer
      - .actual_access:  write_only
        .address_space:  global
        .offset:         24
        .size:           8
        .value_kind:     global_buffer
      - .actual_access:  write_only
        .address_space:  global
        .offset:         32
        .size:           8
        .value_kind:     global_buffer
    .group_segment_fixed_size: 0
    .kernarg_segment_align: 8
    .kernarg_segment_size: 40
    .language:       OpenCL C
    .language_version:
      - 2
      - 0
    .max_flat_workgroup_size: 256
    .name:           _Z6k_prepPKfS0_P6__halfS2_Pi
    .private_segment_fixed_size: 0
    .sgpr_count:     18
    .sgpr_spill_count: 0
    .symbol:         _Z6k_prepPKfS0_P6__halfS2_Pi.kd
    .uniform_work_group_size: 1
    .uses_dynamic_stack: false
    .vgpr_count:     6
    .vgpr_spill_count: 0
    .wavefront_size: 64
  - .agpr_count:     0
    .args:
      - .actual_access:  read_only
        .address_space:  global
        .offset:         0
        .size:           8
        .value_kind:     global_buffer
      - .actual_access:  read_only
        .address_space:  global
        .offset:         8
        .size:           8
        .value_kind:     global_buffer
      - .address_space:  global
        .offset:         16
        .size:           8
        .value_kind:     global_buffer
      - .actual_access:  write_only
        .address_space:  global
        .offset:         24
        .size:           8
        .value_kind:     global_buffer
      - .actual_access:  write_only
        .address_space:  global
        .offset:         32
        .size:           8
        .value_kind:     global_buffer
      - .actual_access:  read_only
        .address_space:  global
        .offset:         40
        .size:           8
        .value_kind:     global_buffer
      - .actual_access:  read_only
        .address_space:  global
        .offset:         48
        .size:           8
        .value_kind:     global_buffer
      - .actual_access:  read_only
        .address_space:  global
        .offset:         56
        .size:           8
        .value_kind:     global_buffer
      - .actual_access:  read_only
        .address_space:  global
        .offset:         64
        .size:           8
        .value_kind:     global_buffer
      - .actual_access:  write_only
        .address_space:  global
        .offset:         72
        .size:           8
        .value_kind:     global_buffer
      - .actual_access:  read_only
        .address_space:  global
        .offset:         80
        .size:           8
        .value_kind:     global_buffer
      - .actual_access:  write_only
        .address_space:  global
        .offset:         88
        .size:           8
        .value_kind:     global_buffer
    .group_segment_fixed_size: 53248
    .kernarg_segment_align: 8
    .kernarg_segment_size: 96
    .language:       OpenCL C
    .language_version:
      - 2
      - 0
    .max_flat_workgroup_size: 256
    .name:           _Z15k_scatter_gemm1PKiS0_PiPjPyPKfPK6__halfS5_S5_PS6_PfSA_
    .private_segment_fixed_size: 0
    .sgpr_count:     32
    .sgpr_spill_count: 0
    .symbol:         _Z15k_scatter_gemm1PKiS0_PiPjPyPKfPK6__halfS5_S5_PS6_PfSA_.kd
    .uniform_work_group_size: 1
    .uses_dynamic_stack: false
    .vgpr_count:     146
    .vgpr_spill_count: 0
    .wavefront_size: 64
  - .agpr_count:     0
    .args:
      - .actual_access:  read_only
        .address_space:  global
        .offset:         0
        .size:           8
        .value_kind:     global_buffer
      - .actual_access:  read_only
        .address_space:  global
        .offset:         8
        .size:           8
        .value_kind:     global_buffer
      - .actual_access:  read_only
        .address_space:  global
        .offset:         16
        .size:           8
        .value_kind:     global_buffer
      - .actual_access:  write_only
        .address_space:  global
        .offset:         24
        .size:           8
        .value_kind:     global_buffer
      - .actual_access:  write_only
        .address_space:  global
        .offset:         32
        .size:           8
        .value_kind:     global_buffer
      - .actual_access:  write_only
        .address_space:  global
        .offset:         40
        .size:           8
        .value_kind:     global_buffer
      - .actual_access:  write_only
        .address_space:  global
        .offset:         48
        .size:           8
        .value_kind:     global_buffer
      - .actual_access:  read_only
        .address_space:  global
        .offset:         56
        .size:           8
        .value_kind:     global_buffer
      - .actual_access:  read_only
        .address_space:  global
        .offset:         64
        .size:           8
        .value_kind:     global_buffer
      - .actual_access:  read_only
        .address_space:  global
        .offset:         72
        .size:           8
        .value_kind:     global_buffer
      - .actual_access:  read_only
        .address_space:  global
        .offset:         80
        .size:           8
        .value_kind:     global_buffer
      - .actual_access:  write_only
        .address_space:  global
        .offset:         88
        .size:           8
        .value_kind:     global_buffer
      - .actual_access:  read_only
        .address_space:  global
        .offset:         96
        .size:           8
        .value_kind:     global_buffer
      - .actual_access:  write_only
        .address_space:  global
        .offset:         104
        .size:           8
        .value_kind:     global_buffer
    .group_segment_fixed_size: 53248
    .kernarg_segment_align: 8
    .kernarg_segment_size: 112
    .language:       OpenCL C
    .language_version:
      - 2
      - 0
    .max_flat_workgroup_size: 256
    .name:           _Z12k_fine_gemm1PKjPKyPKiPiS5_S5_S5_PKfPK6__halfS7_S7_PS8_PfSC_
    .private_segment_fixed_size: 0
    .sgpr_count:     102
    .sgpr_spill_count: 0
    .symbol:         _Z12k_fine_gemm1PKjPKyPKiPiS5_S5_S5_PKfPK6__halfS7_S7_PS8_PfSC_.kd
    .uniform_work_group_size: 1
    .uses_dynamic_stack: false
    .vgpr_count:     144
    .vgpr_spill_count: 0
    .wavefront_size: 64
  - .agpr_count:     0
    .args:
      - .actual_access:  read_only
        .address_space:  global
        .offset:         0
        .size:           8
        .value_kind:     global_buffer
      - .actual_access:  read_only
        .address_space:  global
        .offset:         8
        .size:           8
        .value_kind:     global_buffer
      - .actual_access:  read_only
        .address_space:  global
        .offset:         16
        .size:           8
        .value_kind:     global_buffer
      - .actual_access:  read_only
        .address_space:  global
        .offset:         24
        .size:           8
        .value_kind:     global_buffer
      - .actual_access:  read_only
        .address_space:  global
        .offset:         32
        .size:           8
        .value_kind:     global_buffer
      - .actual_access:  read_only
        .address_space:  global
        .offset:         40
        .size:           8
        .value_kind:     global_buffer
      - .actual_access:  read_only
        .address_space:  global
        .offset:         48
        .size:           8
        .value_kind:     global_buffer
      - .actual_access:  read_only
        .address_space:  global
        .offset:         56
        .size:           8
        .value_kind:     global_buffer
      - .actual_access:  read_only
        .address_space:  global
        .offset:         64
        .size:           8
        .value_kind:     global_buffer
      - .actual_access:  write_only
        .address_space:  global
        .offset:         72
        .size:           8
        .value_kind:     global_buffer
      - .actual_access:  read_only
        .address_space:  global
        .offset:         80
        .size:           8
        .value_kind:     global_buffer
      - .actual_access:  write_only
        .address_space:  global
        .offset:         88
        .size:           8
        .value_kind:     global_buffer
      - .actual_access:  read_only
        .address_space:  global
        .offset:         96
        .size:           8
        .value_kind:     global_buffer
      - .actual_access:  read_only
        .address_space:  global
        .offset:         104
        .size:           8
        .value_kind:     global_buffer
      - .actual_access:  read_only
        .address_space:  global
        .offset:         112
        .size:           8
        .value_kind:     global_buffer
    .group_segment_fixed_size: 5376
    .kernarg_segment_align: 8
    .kernarg_segment_size: 120
    .language:       OpenCL C
    .language_version:
      - 2
      - 0
    .max_flat_workgroup_size: 256
    .name:           _Z6k_agg1PKiS0_PK6__halfPKfS5_S5_S3_S5_S5_PS1_PfS7_S5_S0_S0_
    .private_segment_fixed_size: 0
    .sgpr_count:     44
    .sgpr_spill_count: 0
    .symbol:         _Z6k_agg1PKiS0_PK6__halfPKfS5_S5_S3_S5_S5_PS1_PfS7_S5_S0_S0_.kd
    .uniform_work_group_size: 1
    .uses_dynamic_stack: false
    .vgpr_count:     78
    .vgpr_spill_count: 0
    .wavefront_size: 64
  - .agpr_count:     0
    .args:
      - .actual_access:  read_only
        .address_space:  global
        .offset:         0
        .size:           8
        .value_kind:     global_buffer
      - .actual_access:  read_only
        .address_space:  global
        .offset:         8
        .size:           8
        .value_kind:     global_buffer
      - .actual_access:  read_only
        .address_space:  global
        .offset:         16
        .size:           8
        .value_kind:     global_buffer
      - .actual_access:  read_only
        .address_space:  global
        .offset:         24
        .size:           8
        .value_kind:     global_buffer
      - .actual_access:  read_only
        .address_space:  global
        .offset:         32
        .size:           8
        .value_kind:     global_buffer
      - .actual_access:  read_only
        .address_space:  global
        .offset:         40
        .size:           8
        .value_kind:     global_buffer
      - .actual_access:  write_only
        .address_space:  global
        .offset:         48
        .size:           8
        .value_kind:     global_buffer
      - .actual_access:  read_only
        .address_space:  global
        .offset:         56
        .size:           8
        .value_kind:     global_buffer
      - .actual_access:  read_only
        .address_space:  global
        .offset:         64
        .size:           8
        .value_kind:     global_buffer
      - .actual_access:  read_only
        .address_space:  global
        .offset:         72
        .size:           8
        .value_kind:     global_buffer
    .group_segment_fixed_size: 1024
    .kernarg_segment_align: 8
    .kernarg_segment_size: 80
    .language:       OpenCL C
    .language_version:
      - 2
      - 0
    .max_flat_workgroup_size: 256
    .name:           _Z6k_agg2PKiS0_PK6__halfPKfS5_S5_PfS5_S0_S0_
    .private_segment_fixed_size: 0
    .sgpr_count:     28
    .sgpr_spill_count: 0
    .symbol:         _Z6k_agg2PKiS0_PK6__halfPKfS5_S5_PfS5_S0_S0_.kd
    .uniform_work_group_size: 1
    .uses_dynamic_stack: false
    .vgpr_count:     60
    .vgpr_spill_count: 0
    .wavefront_size: 64
